# attention: static s_setprio 1 for waves 4-7 (KV group 1) during the main loop
# speedup vs baseline: 1.0024x; 1.0024x over previous
.LBB2_18:
	s_or_b64 exec, exec, s[4:5]
	s_add_i32 s4, s52, 2
	s_lshr_b32 s49, s4, 1
	v_or_b32_e32 v99, 4, v89
	s_mov_b32 s48, 1
	s_cmp_eq_u32 s49, 1
	s_cbranch_scc1 .LBB2_32
	v_or_b32_e32 v1, s33, v37
	v_cmp_gt_u32_e64 s[36:37], v37, v31
	v_cmp_lt_u32_e64 s[4:5], v37, v31
	v_or_b32_e32 v31, 2, v1
	v_cmp_gt_u32_e64 s[6:7], v31, v35
	v_or_b32_e32 v31, 3, v1
	v_cmp_gt_u32_e64 s[8:9], v31, v35
	v_or_b32_e32 v31, 16, v1
	v_cmp_gt_u32_e64 s[10:11], v31, v35
	v_or_b32_e32 v31, 17, v1
	v_cmp_gt_u32_e64 s[12:13], v31, v35
	v_or_b32_e32 v31, 18, v1
	v_cmp_gt_u32_e64 s[14:15], v31, v35
	v_or_b32_e32 v31, 19, v1
	v_cmp_gt_u32_e64 s[16:17], v31, v35
	v_or_b32_e32 v31, 32, v1
	v_cmp_gt_u32_e64 s[18:19], v31, v35
	v_or_b32_e32 v31, 33, v1
	v_cmp_gt_u32_e64 s[20:21], v31, v35
	v_or_b32_e32 v31, 34, v1
	v_cmp_gt_u32_e64 s[22:23], v31, v35
	v_or_b32_e32 v31, 35, v1
	v_cmp_gt_u32_e64 s[24:25], v31, v35
	v_or_b32_e32 v31, 48, v1
	v_cmp_gt_u32_e64 s[26:27], v31, v35
	v_or_b32_e32 v31, 49, v1
	v_cmp_gt_u32_e64 s[28:29], v31, v35
	v_or_b32_e32 v31, 50, v1
	v_or_b32_e32 v1, 51, v1
	v_cmp_gt_u32_e64 s[34:35], v1, v35
	v_mov_b32_e32 v1, 0x100
	v_lshl_or_b32 v72, v88, 6, v1
	v_mov_b32_e32 v1, 0x4000
	v_lshl_or_b32 v70, v88, 12, v1
	v_mov_b32_e32 v1, 0x2000
	s_mov_b32 s44, 0x8000
	v_lshl_or_b32 v74, v88, 11, v1
	v_lshlrev_b32_e32 v78, 1, v30
	s_mov_b32 s45, 0x5040100
	v_xor_b32_e32 v1, 0x8000, v5
	v_xor_b32_sdwa v30, s44, v5 dst_sel:DWORD dst_unused:UNUSED_PAD src0_sel:DWORD src1_sel:WORD_1
	v_lshlrev_b32_e32 v101, 6, v33
	v_perm_b32 v33, v30, v1, s45
	v_xor_b32_e32 v1, 0x8000, v4
	v_xor_b32_sdwa v30, s44, v4 dst_sel:DWORD dst_unused:UNUSED_PAD src0_sel:DWORD src1_sel:WORD_1
	v_lshlrev_b32_e32 v76, 1, v32
	v_perm_b32 v32, v30, v1, s45
	v_xor_b32_e32 v1, 0x8000, v3
	v_xor_b32_sdwa v30, s44, v3 dst_sel:DWORD dst_unused:UNUSED_PAD src0_sel:DWORD src1_sel:WORD_1
	v_cmp_gt_u32_e64 s[30:31], v31, v35
	v_perm_b32 v31, v30, v1, s45
	v_xor_b32_e32 v1, 0x8000, v2
	v_xor_b32_sdwa v30, s44, v2 dst_sel:DWORD dst_unused:UNUSED_PAD src0_sel:DWORD src1_sel:WORD_1
	v_lshlrev_b32_e32 v100, 1, v88
	v_mov_b32_e32 v71, 0
	v_lshlrev_b32_e32 v102, 7, v40
	v_lshlrev_b32_e32 v103, 6, v40
	v_lshlrev_b32_e32 v104, 7, v39
	v_lshlrev_b32_e32 v105, 6, v39
	v_lshlrev_b32_e32 v106, 7, v38
	v_lshlrev_b32_e32 v107, 6, v38
	s_movk_i32 s50, 0x5000
	v_lshlrev_b32_e32 v80, 1, v36
	v_lshlrev_b32_e32 v82, 1, v34
	s_mov_b32 s51, 0xff800000
	s_mov_b32 s53, 0x41700000
	v_perm_b32 v30, v30, v1, s45
	v_mov_b32_e32 v108, 0xff800000
	v_readfirstlane_b32 s64, v98
	s_nop 0
	s_and_b32 s64, s64, 0x80000000
	s_or_b32 s64, s64, 0x3f800000
	v_readfirstlane_b32 s65, v88
	s_nop 0
	s_cmp_eq_u32 s65, 0
	s_cbranch_scc1 .Lattn_prio_done
	s_setprio 1
.Lattn_prio_done:
.LBB2_20:
	s_waitcnt vmcnt(0)
	s_barrier
	v_add_u32_e32 v109, 2, v50
	v_cmp_ge_u32_e32 vcc, s52, v109
	s_and_saveexec_b64 s[44:45], vcc
	s_cbranch_execz .LBB2_22
	v_bitop3_b32 v1, s48, 1, v100 bitop3:0x26
	v_mul_u32_u24_e32 v1, 0x5000, v1
	v_lshl_or_b32 v40, v92, 1, v1
	v_lshl_add_u64 v[34:35], v[70:71], 1, s[40:41]
	v_mov_b32_e32 v73, v71
	v_mov_b32_e32 v77, v71
	v_readfirstlane_b32 s46, v40
	v_add_u32_e32 v41, 0x2000, v40
	v_lshl_add_u64 v[36:37], v[72:73], 1, s[42:43]
	v_lshl_add_u64 v[38:39], v[34:35], 0, v[76:77]
	s_mov_b32 m0, s46
	v_mov_b32_e32 v79, v71
	v_readfirstlane_b32 s46, v41
	global_load_lds_dwordx4 v[38:39], off
	v_lshl_add_u64 v[38:39], v[36:37], 0, v[78:79]
	s_mov_b32 m0, s46
	v_mov_b32_e32 v81, v71
	global_load_lds_dwordx4 v[38:39], off
	v_add_u32_e32 v38, 0x1000, v40
	v_lshl_add_u64 v[34:35], v[34:35], 0, v[80:81]
	v_readfirstlane_b32 s46, v38
	s_mov_b32 m0, s46
	v_mov_b32_e32 v83, v71
	global_load_lds_dwordx4 v[34:35], off
	v_lshl_add_u64 v[34:35], v[36:37], 0, v[82:83]
	v_add_u32_e32 v36, 0x3000, v40
	v_or_b32_e32 v1, v1, v93
	v_readfirstlane_b32 s46, v36
	v_add_u32_e32 v1, 0x4000, v1
	s_mov_b32 m0, s46
	v_mov_b32_e32 v75, v71
	v_readfirstlane_b32 s46, v1
	global_load_lds_dwordx4 v[34:35], off
	v_lshl_add_u64 v[34:35], v[74:75], 1, v[66:67]
	s_mov_b32 m0, s46
	s_nop 0
	global_load_lds_dwordx4 v[34:35], off

.LBB2_32:
	s_setprio 0
	v_cmp_ne_u32_e32 vcc, 0, v88
	s_waitcnt vmcnt(0) lgkmcnt(0)
	s_barrier
	s_and_saveexec_b64 s[4:5], vcc
	s_cbranch_execz .LBB2_34
	v_mul_u32_u24_e32 v1, 0x1200, v91
	v_lshl_or_b32 v1, v87, 2, v1
	ds_write2st64_b32 v1, v69, v68 offset1:1
	ds_write2st64_b32 v1, v26, v27 offset0:2 offset1:3
	ds_write2st64_b32 v1, v28, v29 offset0:4 offset1:5
	ds_write2st64_b32 v1, v22, v23 offset0:6 offset1:7
	ds_write2st64_b32 v1, v24, v25 offset0:8 offset1:9
	ds_write2st64_b32 v1, v18, v19 offset0:10 offset1:11
	ds_write2st64_b32 v1, v20, v21 offset0:12 offset1:13
	ds_write2st64_b32 v1, v14, v15 offset0:14 offset1:15
	ds_write2st64_b32 v1, v16, v17 offset0:16 offset1:17

amdhsa.kernels:
  - .agpr_count:     0
    .args:
      - .actual_access:  read_only
        .address_space:  global
        .offset:         0
        .size:           8
        .value_kind:     global_buffer
      - .actual_access:  read_only
        .address_space:  global
        .offset:         8
        .size:           8
        .value_kind:     global_buffer
      - .actual_access:  read_only
        .address_space:  global
        .offset:         16
        .size:           8
        .value_kind:     global_buffer
      - .actual_access:  read_only
        .address_space:  global
        .offset:         24
        .size:           8
        .value_kind:     global_buffer
      - .actual_access:  read_only
        .address_space:  global
        .offset:         32
        .size:           8
        .value_kind:     global_buffer
      - .actual_access:  read_only
        .address_space:  global
        .offset:         40
        .size:           8
        .value_kind:     global_buffer
      - .actual_access:  read_only
        .address_space:  global
        .offset:         48
        .size:           8
        .value_kind:     global_buffer
      - .address_space:  global
        .offset:         56
        .size:           8
        .value_kind:     global_buffer
      - .address_space:  global
        .offset:         64
        .size:           8
        .value_kind:     global_buffer
      - .actual_access:  read_only
        .address_space:  global
        .offset:         72
        .size:           8
        .value_kind:     global_buffer
      - .address_space:  global
        .offset:         80
        .size:           8
        .value_kind:     global_buffer
    .group_segment_fixed_size: 0
    .kernarg_segment_align: 8
    .kernarg_segment_size: 88
    .language:       OpenCL C
    .language_version:
      - 2
      - 0
    .max_flat_workgroup_size: 256
    .name:           _Z11prep_kernelPKfS0_S0_S0_S0_S0_S0_PDF16_S1_S1_S1_
    .private_segment_fixed_size: 0
    .sgpr_count:     23
    .sgpr_spill_count: 0
    .symbol:         _Z11prep_kernelPKfS0_S0_S0_S0_S0_S0_PDF16_S1_S1_S1_.kd
    .uniform_work_group_size: 1
    .uses_dynamic_stack: false
    .vgpr_count:     28
    .vgpr_spill_count: 0
    .wavefront_size: 64
  - .agpr_count:     0
    .args:
      - .offset:         0
        .size:           88
        .value_kind:     by_value
    .group_segment_fixed_size: 163840
    .kernarg_segment_align: 8
    .kernarg_segment_size: 88
    .language:       OpenCL C
    .language_version:
      - 2
      - 0
    .max_flat_workgroup_size: 512
    .name:           _Z12gemm1_kernel6G1Args
    .private_segment_fixed_size: 0
    .sgpr_count:     58
    .sgpr_spill_count: 0
    .symbol:         _Z12gemm1_kernel6G1Args.kd
    .uniform_work_group_size: 1
    .uses_dynamic_stack: false
    .vgpr_count:     240
    .vgpr_spill_count: 0
    .wavefront_size: 64
  - .agpr_count:     0
    .args:
      - .address_space:  global
        .offset:         0
        .size:           8
        .value_kind:     global_buffer
      - .address_space:  global
        .offset:         8
        .size:           8
        .value_kind:     global_buffer
      - .address_space:  global
        .offset:         16
        .size:           8
        .value_kind:     global_buffer
      - .actual_access:  read_only
        .address_space:  global
        .offset:         24
        .size:           8
        .value_kind:     global_buffer
      - .actual_access:  read_only
        .address_space:  global
        .offset:         32
        .size:           8
        .value_kind:     global_buffer
      - .actual_access:  read_only
        .address_space:  global
        .offset:         40
        .size:           8
        .value_kind:     global_buffer
      - .address_space:  global
        .offset:         48
        .size:           8
        .value_kind:     global_buffer
      - .actual_access:  read_only
        .address_space:  global
        .offset:         56
        .size:           8
        .value_kind:     global_buffer
      - .address_space:  global
        .offset:         64
        .size:           8
        .value_kind:     global_buffer
      - .actual_access:  read_only
        .address_space:  global
        .offset:         72
        .size:           8
        .value_kind:     global_buffer
      - .address_space:  global
        .offset:         80
        .size:           8
        .value_kind:     global_buffer
    .group_segment_fixed_size: 81920
    .kernarg_segment_align: 8
    .kernarg_segment_size: 88
    .language:       OpenCL C
    .language_version:
      - 2
      - 0
    .max_flat_workgroup_size: 512
    .name:           _Z11attn_kernelPKDF16_S0_S0_PKfS2_S2_S0_S2_PDF16_S2_S3_
    .private_segment_fixed_size: 0
    .sgpr_count:     72
    .sgpr_spill_count: 0
    .symbol:         _Z11attn_kernelPKDF16_S0_S0_PKfS2_S2_S0_S2_PDF16_S2_S3_.kd
    .uniform_work_group_size: 1
    .uses_dynamic_stack: false
    .vgpr_count:     126
    .vgpr_spill_count: 0
    .wavefront_size: 64
  - .agpr_count:     0
    .args:
      - .address_space:  global
        .offset:         0
        .size:           8
        .value_kind:     global_buffer
      - .address_space:  global
        .offset:         8
        .size:           8
        .value_kind:     global_buffer
      - .actual_access:  read_only
        .address_space:  global
        .offset:         16
        .size:           8
        .value_kind:     global_buffer
      - .actual_access:  write_only
        .address_space:  global
        .offset:         24
        .size:           8
        .value_kind:     global_buffer
    .group_segment_fixed_size: 122880
    .kernarg_segment_align: 8
    .kernarg_segment_size: 32
    .language:       OpenCL C
    .language_version:
      - 2
      - 0
    .max_flat_workgroup_size: 512
    .name:           _Z14outproj_kernelPKDF16_S0_PKfPf
    .private_segment_fixed_size: 0
    .sgpr_count:     31
    .sgpr_spill_count: 0
    .symbol:         _Z14outproj_kernelPKDF16_S0_PKfPf.kd
    .uniform_work_group_size: 1
    .uses_dynamic_stack: false
    .vgpr_count:     132
    .vgpr_spill_count: 0
    .wavefront_size: 64
